# adds: LN1 router first-half weight fragments kept resident (16 redundant per-group fragment loads removed)
# speedup vs baseline: 1.0164x; 1.0164x over previous
; #define LAS __attribute__((address_space(3)))
; __device__ __forceinline__ void phase_ln1(Frame& F0, const Args& A, int l, bool v_from_h) {
;     ...
;         if (g + F.G < ngroups) { LN1_GLDK(0); LN1_GLDK(1); }
;         {
;             float score[2]; unsigned key[2]; int rank[2] = {0, 0};
; #pragma unroll
;             for (int rr = 0; rr < 2; ++rr) { score[rr] = __builtin_amdgcn_rcpf(1.0f + __expf(-LOG[(2 * wave + rr) * 64 + lane]));
;                 key[rr] = (__float_as_uint(score[rr] + brl + 2.0f) & ~63u) | (unsigned)(63 - lane);
;                 KEYS[(2 * wave + rr) * 64 + lane] = key[rr]; }
; #pragma unroll
;             for (int i = 0; i < 16; ++i) {
; #pragma unroll
;                 for (int rr = 0; rr < 2; ++rr) { const v4u kq = *(const LAS v4u*)(KEYS + (2 * wave + rr) * 64 + 4 * i);
;                     rank[rr] += (int)(kq.x > key[rr]) + (int)(kq.y > key[rr]) + (int)(kq.z > key[rr]) + (int)(kq.w > key[rr]); } }
.LBB0_1296:
	s_waitcnt lgkmcnt(0)
	s_barrier
	s_andn2_b64 vcc, exec, s[14:15]
	s_cbranch_vccnz .LBB0_1298
.LBB0_1298:
	ds_read_b32 v64, v226
	ds_read_b32 v65, v228
	v_mov_b32_e32 v162, s44
	v_mov_b32_e32 v180, -1
	s_waitcnt lgkmcnt(1)
	v_mul_f32_e32 v64, 0xbfb8aa3b, v64
	s_waitcnt lgkmcnt(0)
	v_mul_f32_e32 v65, 0xbfb8aa3b, v65
	v_exp_f32_e32 v64, v64
	v_exp_f32_e32 v65, v65
	v_add_f32_e32 v64, 1.0, v64
	v_add_f32_e32 v65, 1.0, v65
	v_rcp_f32_e32 v165, v64
	v_rcp_f32_e32 v164, v65
	s_nop 0
	v_pk_add_f32 v[64:65], v[148:149], v[164:165]
	s_nop 0
	v_pk_add_f32 v[64:65], v[64:65], 2.0 op_sel_hi:[1,0]
	s_nop 0
	v_and_b32_e32 v65, 0xffffffc0, v65
	v_and_b32_e32 v64, 0xffffffc0, v64
	v_or_b32_e32 v170, v65, v129
	v_or_b32_e32 v163, v64, v160
	ds_write_b32 v227, v170
	ds_write_b32 v229, v163
	ds_read_b128 v[64:67], v162
	ds_read_b128 v[68:71], v162 offset:16
	ds_read_b128 v[76:79], v162 offset:32
	ds_read_b128 v[80:83], v162 offset:48
	s_waitcnt lgkmcnt(3)
	v_cmp_gt_u32_e32 vcc, v64, v170
	s_nop 1
	v_cndmask_b32_e64 v64, 0, 1, vcc
	v_cmp_gt_u32_e32 vcc, v66, v170
	s_nop 1
	v_cndmask_b32_e64 v66, 0, 1, vcc
	v_cmp_gt_u32_e32 vcc, v65, v170
	s_nop 1
	v_addc_co_u32_e32 v64, vcc, 0, v64, vcc
	v_cmp_gt_u32_e32 vcc, v67, v170
	s_nop 1
	v_addc_co_u32_e32 v64, vcc, v64, v66, vcc
	s_waitcnt lgkmcnt(2)
	v_cmp_gt_u32_e32 vcc, v69, v170
	s_nop 1
	v_cndmask_b32_e64 v65, 0, 1, vcc
	v_cmp_gt_u32_e32 vcc, v70, v170
	s_nop 1
	v_cndmask_b32_e64 v66, 0, 1, vcc
	v_cmp_gt_u32_e32 vcc, v68, v170
	s_nop 1
	v_addc_co_u32_e32 v64, vcc, v64, v65, vcc
	v_cmp_gt_u32_e32 vcc, v71, v170
	s_nop 1
	v_addc_co_u32_e32 v68, vcc, v64, v66, vcc
	s_waitcnt lgkmcnt(1)
	v_cmp_gt_u32_e32 vcc, v77, v170
	ds_read_b128 v[72:75], v162 offset:256
	ds_read_b128 v[64:67], v162 offset:272
	v_cndmask_b32_e64 v69, 0, 1, vcc
	v_cmp_gt_u32_e32 vcc, v78, v170
	ds_read_b128 v[84:87], v162 offset:64
	s_nop 0
	v_cndmask_b32_e64 v70, 0, 1, vcc
	v_cmp_gt_u32_e32 vcc, v76, v170
	s_nop 1
	v_addc_co_u32_e32 v68, vcc, v68, v69, vcc
	v_cmp_gt_u32_e32 vcc, v79, v170
	s_nop 1
	v_addc_co_u32_e32 v68, vcc, v68, v70, vcc
	s_waitcnt lgkmcnt(3)
	v_cmp_gt_u32_e32 vcc, v81, v170
	s_nop 1
	v_cndmask_b32_e64 v69, 0, 1, vcc
	v_cmp_gt_u32_e32 vcc, v82, v170
	s_nop 1
	v_cndmask_b32_e64 v70, 0, 1, vcc
	v_cmp_gt_u32_e32 vcc, v80, v170
	s_nop 1
	v_addc_co_u32_e32 v68, vcc, v68, v69, vcc
	v_cmp_gt_u32_e32 vcc, v83, v170
	s_nop 1
	v_addc_co_u32_e32 v88, vcc, v68, v70, vcc
	s_waitcnt lgkmcnt(0)
	v_cmp_gt_u32_e32 vcc, v85, v170
	ds_read_b128 v[76:79], v162 offset:288
	ds_read_b128 v[68:71], v162 offset:304
	ds_read_b128 v[80:83], v162 offset:80
	v_cndmask_b32_e64 v85, 0, 1, vcc
	v_cmp_gt_u32_e32 vcc, v86, v170
	s_nop 1
	v_cndmask_b32_e64 v86, 0, 1, vcc
	v_cmp_gt_u32_e32 vcc, v84, v170
	s_nop 1
	v_addc_co_u32_e32 v84, vcc, v88, v85, vcc
	v_cmp_gt_u32_e32 vcc, v87, v170
	ds_read_b128 v[88:91], v162 offset:96
	s_nop 0
	v_addc_co_u32_e32 v84, vcc, v84, v86, vcc
	s_waitcnt lgkmcnt(1)
	v_cmp_gt_u32_e32 vcc, v81, v170
	s_nop 1
	v_cndmask_b32_e64 v81, 0, 1, vcc
	v_cmp_gt_u32_e32 vcc, v82, v170
	s_nop 1
	v_cndmask_b32_e64 v82, 0, 1, vcc
	v_cmp_gt_u32_e32 vcc, v80, v170
	s_nop 1
	v_addc_co_u32_e32 v80, vcc, v84, v81, vcc
	v_cmp_gt_u32_e32 vcc, v83, v170
	s_nop 1
	v_addc_co_u32_e32 v96, vcc, v80, v82, vcc
	s_waitcnt lgkmcnt(0)
	v_cmp_gt_u32_e32 vcc, v89, v170
	ds_read_b128 v[84:87], v162 offset:320
	ds_read_b128 v[80:83], v162 offset:336
	ds_read_b128 v[92:95], v162 offset:112
	v_cndmask_b32_e64 v89, 0, 1, vcc
	v_cmp_gt_u32_e32 vcc, v90, v170
	s_nop 1
	v_cndmask_b32_e64 v90, 0, 1, vcc
	v_cmp_gt_u32_e32 vcc, v88, v170
	s_nop 1
	v_addc_co_u32_e32 v88, vcc, v96, v89, vcc
	v_cmp_gt_u32_e32 vcc, v91, v170
	ds_read_b128 v[96:99], v162 offset:128
	s_nop 0
	v_addc_co_u32_e32 v88, vcc, v88, v90, vcc
	s_waitcnt lgkmcnt(1)
	v_cmp_gt_u32_e32 vcc, v93, v170
	s_nop 1
	v_cndmask_b32_e64 v89, 0, 1, vcc
	v_cmp_gt_u32_e32 vcc, v94, v170
	s_nop 1
	v_cndmask_b32_e64 v90, 0, 1, vcc
	v_cmp_gt_u32_e32 vcc, v92, v170
	s_nop 1
	v_addc_co_u32_e32 v88, vcc, v88, v89, vcc
	v_cmp_gt_u32_e32 vcc, v95, v170
	s_nop 1
	v_addc_co_u32_e32 v104, vcc, v88, v90, vcc
	s_waitcnt lgkmcnt(0)
	v_cmp_gt_u32_e32 vcc, v97, v170
	ds_read_b128 v[92:95], v162 offset:352
	ds_read_b128 v[88:91], v162 offset:368
	ds_read_b128 v[100:103], v162 offset:144
	v_cndmask_b32_e64 v97, 0, 1, vcc
	v_cmp_gt_u32_e32 vcc, v98, v170
	s_nop 1
	v_cndmask_b32_e64 v98, 0, 1, vcc
	v_cmp_gt_u32_e32 vcc, v96, v170
	s_nop 1
	v_addc_co_u32_e32 v96, vcc, v104, v97, vcc
	v_cmp_gt_u32_e32 vcc, v99, v170
	ds_read_b128 v[104:107], v162 offset:160
	s_nop 0
	v_addc_co_u32_e32 v96, vcc, v96, v98, vcc
	s_waitcnt lgkmcnt(1)
	v_cmp_gt_u32_e32 vcc, v101, v170
	s_nop 1
	v_cndmask_b32_e64 v97, 0, 1, vcc
	v_cmp_gt_u32_e32 vcc, v102, v170
	s_nop 1
	v_cndmask_b32_e64 v98, 0, 1, vcc
	v_cmp_gt_u32_e32 vcc, v100, v170
	s_nop 1
	v_addc_co_u32_e32 v96, vcc, v96, v97, vcc
	v_cmp_gt_u32_e32 vcc, v103, v170
	s_nop 1
	v_addc_co_u32_e32 v112, vcc, v96, v98, vcc
	s_waitcnt lgkmcnt(0)
	v_cmp_gt_u32_e32 vcc, v105, v170
	ds_read_b128 v[100:103], v162 offset:384
	ds_read_b128 v[96:99], v162 offset:400
	ds_read_b128 v[108:111], v162 offset:176
	v_cndmask_b32_e64 v105, 0, 1, vcc
	v_cmp_gt_u32_e32 vcc, v106, v170
	s_nop 1
	v_cndmask_b32_e64 v106, 0, 1, vcc
	v_cmp_gt_u32_e32 vcc, v104, v170
	s_nop 1
	v_addc_co_u32_e32 v104, vcc, v112, v105, vcc
	v_cmp_gt_u32_e32 vcc, v107, v170
	ds_read_b128 v[112:115], v162 offset:192
	s_nop 0
	v_addc_co_u32_e32 v104, vcc, v104, v106, vcc
	s_waitcnt lgkmcnt(1)
; #define LAS __attribute__((address_space(3)))
; __device__ __forceinline__ void phase_ln1(Frame& F0, const Args& A, int l, bool v_from_h) {
;     ...
;             for (int i = 0; i < 16; ++i) {
; #pragma unroll
;                 for (int rr = 0; rr < 2; ++rr) { const v4u kq = *(const LAS v4u*)(KEYS + (2 * wave + rr) * 64 + 4 * i);
;                     rank[rr] += (int)(kq.x > key[rr]) + (int)(kq.y > key[rr]) + (int)(kq.z > key[rr]) + (int)(kq.w > key[rr]); } }
; #pragma unroll
;             for (int rr = 0; rr < 2; ++rr) { const bool sel = rank[rr] < 8; const float ssum = wave_sum(sel ? score[rr] : 0.f);
;                 pend_r[rr] = sel ? rank[rr] : -1; pend_w[rr] = score[rr] / ssum * ROUTED_SCALE; if (sel) atomicAdd((int*)&lhist[lane], 1); }
	v_cmp_gt_u32_e32 vcc, v109, v170
	s_nop 1
	v_cndmask_b32_e64 v105, 0, 1, vcc
	v_cmp_gt_u32_e32 vcc, v110, v170
	s_nop 1
	v_cndmask_b32_e64 v106, 0, 1, vcc
	v_cmp_gt_u32_e32 vcc, v108, v170
	s_nop 1
	v_addc_co_u32_e32 v104, vcc, v104, v105, vcc
	v_cmp_gt_u32_e32 vcc, v111, v170
	s_nop 1
	v_addc_co_u32_e32 v120, vcc, v104, v106, vcc
	s_waitcnt lgkmcnt(0)
	v_cmp_gt_u32_e32 vcc, v113, v170
	ds_read_b128 v[108:111], v162 offset:416
	ds_read_b128 v[104:107], v162 offset:432
	ds_read_b128 v[116:119], v162 offset:208
	v_cndmask_b32_e64 v113, 0, 1, vcc
	v_cmp_gt_u32_e32 vcc, v114, v170
	ds_read_b128 v[124:127], v162 offset:224
	s_nop 0
	v_cndmask_b32_e64 v114, 0, 1, vcc
	v_cmp_gt_u32_e32 vcc, v112, v170
	s_nop 1
	v_addc_co_u32_e32 v112, vcc, v120, v113, vcc
	v_cmp_gt_u32_e32 vcc, v115, v170
	s_nop 1
	v_addc_co_u32_e32 v112, vcc, v112, v114, vcc
	s_waitcnt lgkmcnt(1)
	v_cmp_gt_u32_e32 vcc, v117, v170
	s_nop 1
	v_cndmask_b32_e64 v113, 0, 1, vcc
	v_cmp_gt_u32_e32 vcc, v118, v170
	s_nop 1
	v_cndmask_b32_e64 v114, 0, 1, vcc
	v_cmp_gt_u32_e32 vcc, v116, v170
	s_nop 1
	v_addc_co_u32_e32 v112, vcc, v112, v113, vcc
	v_cmp_gt_u32_e32 vcc, v119, v170
	s_nop 1
	v_addc_co_u32_e32 v116, vcc, v112, v114, vcc
	s_waitcnt lgkmcnt(0)
	v_cmp_gt_u32_e32 vcc, v125, v170
	ds_read_b128 v[120:123], v162 offset:448
	ds_read_b128 v[112:115], v162 offset:464
	ds_read_b128 v[166:169], v162 offset:240
	v_cndmask_b32_e64 v117, 0, 1, vcc
	v_cmp_gt_u32_e32 vcc, v126, v170
	s_waitcnt lgkmcnt(0)
	v_cmp_gt_u32_e64 s[40:41], v166, v170
	v_cndmask_b32_e64 v118, 0, 1, vcc
	v_cmp_gt_u32_e32 vcc, v124, v170
	v_mov_b32_e32 v166, v181
	s_nop 0
	v_addc_co_u32_e32 v116, vcc, v116, v117, vcc
	v_cmp_gt_u32_e32 vcc, v127, v170
	s_nop 1
	v_addc_co_u32_e32 v171, vcc, v116, v118, vcc
	ds_read_b128 v[124:127], v162 offset:480
	ds_read_b128 v[116:119], v162 offset:496
	v_cmp_gt_u32_e32 vcc, v167, v170
	s_nop 1
	v_cndmask_b32_e64 v162, 0, 1, vcc
	v_cmp_gt_u32_e32 vcc, v168, v170
	s_nop 1
	v_cndmask_b32_e64 v167, 0, 1, vcc
	s_waitcnt lgkmcnt(0)
	v_cmp_gt_u32_e32 vcc, v116, v163
	v_addc_co_u32_e64 v116, s[40:41], v171, v162, s[40:41]
	v_cmp_gt_u32_e64 s[40:41], v169, v170
	s_nop 1
	v_addc_co_u32_e64 v116, s[40:41], v116, v167, s[40:41]
	v_cmp_gt_u32_e64 s[40:41], 8, v116
	s_nop 1
	v_cndmask_b32_e64 v162, 0, v165, s[40:41]
	s_nop 1
	v_add_f32_dpp v162, v162, v162 row_shr:1 row_mask:0xf bank_mask:0xf bound_ctrl:1
	s_nop 1
	v_add_f32_dpp v162, v162, v162 row_shr:2 row_mask:0xf bank_mask:0xf bound_ctrl:1
	s_nop 1
	v_add_f32_dpp v162, v162, v162 row_shr:4 row_mask:0xf bank_mask:0xf bound_ctrl:1
	s_nop 1
	v_add_f32_dpp v162, v162, v162 row_shr:8 row_mask:0xf bank_mask:0xf bound_ctrl:1
	s_nop 1
	v_mov_b32_dpp v166, v162 row_bcast:15 row_mask:0xa bank_mask:0xf
	v_add_f32_e32 v162, v162, v166
	v_mov_b32_e32 v166, v181
	s_nop 1
	v_mov_b32_dpp v166, v162 row_bcast:31 row_mask:0xc bank_mask:0xf
	v_add_f32_e32 v162, v162, v166
	s_nop 0
	v_readlane_b32 s2, v162, 63
	v_mov_b32_e32 v162, -1
	s_and_saveexec_b64 s[0:1], s[40:41]
	ds_add_u32 v223, v216
	v_mov_b32_e32 v180, v116
	s_or_b64 exec, exec, s[0:1]
	v_cmp_gt_u32_e64 s[40:41], v72, v163
	s_nop 1
	v_cndmask_b32_e64 v72, 0, 1, s[40:41]
	v_cmp_gt_u32_e64 s[40:41], v73, v163
	s_nop 1
	v_cndmask_b32_e64 v73, 0, 1, s[40:41]
	v_cmp_gt_u32_e64 s[40:41], v75, v163
	s_nop 1
	v_cndmask_b32_e64 v75, 0, 1, s[40:41]
	v_cmp_gt_u32_e64 s[40:41], v74, v163
	s_nop 1
	v_addc_co_u32_e64 v72, s[40:41], v73, v72, s[40:41]
	v_cmp_gt_u32_e64 s[40:41], v64, v163
	s_nop 1
	v_cndmask_b32_e64 v64, 0, 1, s[40:41]
	v_cmp_gt_u32_e64 s[40:41], v67, v163
	s_nop 1
	v_cndmask_b32_e64 v67, 0, 1, s[40:41]
	v_cmp_gt_u32_e64 s[40:41], v65, v163
	s_nop 1
	v_addc_co_u32_e64 v65, s[40:41], v72, v75, s[40:41]
	v_cmp_gt_u32_e64 s[40:41], v66, v163
	s_nop 1
	v_addc_co_u32_e64 v64, s[40:41], v65, v64, s[40:41]
	v_cmp_gt_u32_e64 s[40:41], v76, v163
	s_nop 1
	v_cndmask_b32_e64 v65, 0, 1, s[40:41]
	v_cmp_gt_u32_e64 s[40:41], v79, v163
	s_nop 1
	v_cndmask_b32_e64 v66, 0, 1, s[40:41]
	v_cmp_gt_u32_e64 s[40:41], v77, v163
	s_nop 1
	v_addc_co_u32_e64 v64, s[40:41], v64, v67, s[40:41]
	v_cmp_gt_u32_e64 s[40:41], v78, v163
	s_nop 1
	v_addc_co_u32_e64 v64, s[40:41], v64, v65, s[40:41]
	v_cmp_gt_u32_e64 s[40:41], v68, v163
	s_nop 1
	v_cndmask_b32_e64 v65, 0, 1, s[40:41]
	v_cmp_gt_u32_e64 s[40:41], v71, v163
	s_nop 1
	v_cndmask_b32_e64 v67, 0, 1, s[40:41]
	v_cmp_gt_u32_e64 s[40:41], v69, v163
	s_nop 1
	v_addc_co_u32_e64 v64, s[40:41], v64, v66, s[40:41]
	v_cmp_gt_u32_e64 s[40:41], v70, v163
	s_nop 1
	v_addc_co_u32_e64 v64, s[40:41], v64, v65, s[40:41]
	v_cmp_gt_u32_e64 s[40:41], v84, v163
	s_nop 1
	v_cndmask_b32_e64 v65, 0, 1, s[40:41]
	v_cmp_gt_u32_e64 s[40:41], v87, v163
	s_nop 1
	v_cndmask_b32_e64 v66, 0, 1, s[40:41]
	v_cmp_gt_u32_e64 s[40:41], v85, v163
	s_nop 1
	v_addc_co_u32_e64 v64, s[40:41], v64, v67, s[40:41]
	v_cmp_gt_u32_e64 s[40:41], v86, v163
	s_nop 1
	v_addc_co_u32_e64 v64, s[40:41], v64, v65, s[40:41]
; #define LAS __attribute__((address_space(3)))
; __device__ __forceinline__ void phase_ln1(Frame& F0, const Args& A, int l, bool v_from_h) {
;     ...
;             for (int i = 0; i < 16; ++i) {
; #pragma unroll
;                 for (int rr = 0; rr < 2; ++rr) { const v4u kq = *(const LAS v4u*)(KEYS + (2 * wave + rr) * 64 + 4 * i);
;                     rank[rr] += (int)(kq.x > key[rr]) + (int)(kq.y > key[rr]) + (int)(kq.z > key[rr]) + (int)(kq.w > key[rr]); } }
; #pragma unroll
;             for (int rr = 0; rr < 2; ++rr) { const bool sel = rank[rr] < 8; const float ssum = wave_sum(sel ? score[rr] : 0.f);
;                 pend_r[rr] = sel ? rank[rr] : -1; pend_w[rr] = score[rr] / ssum * ROUTED_SCALE; if (sel) atomicAdd((int*)&lhist[lane], 1); }
	v_cmp_gt_u32_e64 s[40:41], v80, v163
	s_nop 1
	v_cndmask_b32_e64 v65, 0, 1, s[40:41]
	v_cmp_gt_u32_e64 s[40:41], v83, v163
	s_nop 1
	v_cndmask_b32_e64 v67, 0, 1, s[40:41]
	v_cmp_gt_u32_e64 s[40:41], v81, v163
	s_nop 1
	v_addc_co_u32_e64 v64, s[40:41], v64, v66, s[40:41]
	v_cmp_gt_u32_e64 s[40:41], v82, v163
	s_nop 1
	v_addc_co_u32_e64 v64, s[40:41], v64, v65, s[40:41]
	v_cmp_gt_u32_e64 s[40:41], v92, v163
	s_nop 1
	v_cndmask_b32_e64 v65, 0, 1, s[40:41]
	v_cmp_gt_u32_e64 s[40:41], v95, v163
	s_nop 1
	v_cndmask_b32_e64 v66, 0, 1, s[40:41]
	v_cmp_gt_u32_e64 s[40:41], v93, v163
	s_nop 1
	v_addc_co_u32_e64 v64, s[40:41], v64, v67, s[40:41]
	v_cmp_gt_u32_e64 s[40:41], v94, v163
	s_nop 1
	v_addc_co_u32_e64 v64, s[40:41], v64, v65, s[40:41]
	v_cmp_gt_u32_e64 s[40:41], v88, v163
	s_nop 1
	v_cndmask_b32_e64 v65, 0, 1, s[40:41]
	v_cmp_gt_u32_e64 s[40:41], v91, v163
	s_nop 1
	v_cndmask_b32_e64 v67, 0, 1, s[40:41]
	v_cmp_gt_u32_e64 s[40:41], v89, v163
	s_nop 1
	v_addc_co_u32_e64 v64, s[40:41], v64, v66, s[40:41]
	v_cmp_gt_u32_e64 s[40:41], v90, v163
	s_nop 1
	v_addc_co_u32_e64 v64, s[40:41], v64, v65, s[40:41]
	v_cmp_gt_u32_e64 s[40:41], v100, v163
	s_nop 1
	v_cndmask_b32_e64 v65, 0, 1, s[40:41]
	v_cmp_gt_u32_e64 s[40:41], v103, v163
	s_nop 1
	v_cndmask_b32_e64 v66, 0, 1, s[40:41]
	v_cmp_gt_u32_e64 s[40:41], v101, v163
	s_nop 1
	v_addc_co_u32_e64 v64, s[40:41], v64, v67, s[40:41]
	v_cmp_gt_u32_e64 s[40:41], v102, v163
	s_nop 1
	v_addc_co_u32_e64 v64, s[40:41], v64, v65, s[40:41]
	v_cmp_gt_u32_e64 s[40:41], v96, v163
	s_nop 1
	v_cndmask_b32_e64 v65, 0, 1, s[40:41]
	v_cmp_gt_u32_e64 s[40:41], v99, v163
	s_nop 1
	v_cndmask_b32_e64 v67, 0, 1, s[40:41]
	v_cmp_gt_u32_e64 s[40:41], v97, v163
	s_nop 1
	v_addc_co_u32_e64 v64, s[40:41], v64, v66, s[40:41]
	v_cmp_gt_u32_e64 s[40:41], v98, v163
	s_nop 1
	v_addc_co_u32_e64 v64, s[40:41], v64, v65, s[40:41]
	v_cmp_gt_u32_e64 s[40:41], v108, v163
	s_nop 1
	v_cndmask_b32_e64 v65, 0, 1, s[40:41]
	v_cmp_gt_u32_e64 s[40:41], v111, v163
	s_nop 1
	v_cndmask_b32_e64 v66, 0, 1, s[40:41]
	v_cmp_gt_u32_e64 s[40:41], v109, v163
	s_nop 1
	v_addc_co_u32_e64 v64, s[40:41], v64, v67, s[40:41]
	v_cmp_gt_u32_e64 s[40:41], v110, v163
	s_nop 1
	v_addc_co_u32_e64 v64, s[40:41], v64, v65, s[40:41]
	v_cmp_gt_u32_e64 s[40:41], v104, v163
	s_nop 1
	v_cndmask_b32_e64 v65, 0, 1, s[40:41]
	v_cmp_gt_u32_e64 s[40:41], v107, v163
	s_nop 1
	v_cndmask_b32_e64 v67, 0, 1, s[40:41]
	v_cmp_gt_u32_e64 s[40:41], v105, v163
	s_nop 1
	v_addc_co_u32_e64 v64, s[40:41], v64, v66, s[40:41]
	v_cmp_gt_u32_e64 s[40:41], v106, v163
	s_nop 1
	v_addc_co_u32_e64 v64, s[40:41], v64, v65, s[40:41]
	v_cmp_gt_u32_e64 s[40:41], v120, v163
	s_nop 1
	v_cndmask_b32_e64 v65, 0, 1, s[40:41]
	v_cmp_gt_u32_e64 s[40:41], v123, v163
	s_nop 1
	v_cndmask_b32_e64 v66, 0, 1, s[40:41]
	v_cmp_gt_u32_e64 s[40:41], v121, v163
	s_nop 1
	v_addc_co_u32_e64 v64, s[40:41], v64, v67, s[40:41]
	v_cmp_gt_u32_e64 s[40:41], v122, v163
	s_nop 1
	v_addc_co_u32_e64 v64, s[40:41], v64, v65, s[40:41]
	v_cmp_gt_u32_e64 s[40:41], v112, v163
	s_nop 1
	v_cndmask_b32_e64 v65, 0, 1, s[40:41]
	v_cmp_gt_u32_e64 s[40:41], v115, v163
	s_nop 1
	v_cndmask_b32_e64 v67, 0, 1, s[40:41]
	v_cmp_gt_u32_e64 s[40:41], v113, v163
	s_nop 1
	v_addc_co_u32_e64 v64, s[40:41], v64, v66, s[40:41]
	v_cmp_gt_u32_e64 s[40:41], v114, v163
	s_nop 1
	v_addc_co_u32_e64 v64, s[40:41], v64, v65, s[40:41]
	v_cmp_gt_u32_e64 s[40:41], v124, v163
	s_nop 1
	v_cndmask_b32_e64 v65, 0, 1, s[40:41]
	v_cmp_gt_u32_e64 s[40:41], v127, v163
	s_nop 1
	v_cndmask_b32_e64 v66, 0, 1, s[40:41]
	v_cmp_gt_u32_e64 s[40:41], v125, v163
	s_nop 1
	v_addc_co_u32_e64 v64, s[40:41], v64, v67, s[40:41]
	v_cmp_gt_u32_e64 s[40:41], v126, v163
	s_nop 1
	v_addc_co_u32_e64 v64, s[40:41], v64, v65, s[40:41]
	v_cndmask_b32_e64 v65, 0, 1, vcc
	v_cmp_gt_u32_e32 vcc, v118, v163
	s_nop 1
	v_cndmask_b32_e64 v67, 0, 1, vcc
	v_cmp_gt_u32_e32 vcc, v117, v163
	s_nop 1
	v_addc_co_u32_e32 v64, vcc, v64, v66, vcc
	v_add_u32_e32 v64, v64, v65
	v_cmp_gt_u32_e32 vcc, v119, v163
	v_mov_b32_e32 v66, v181
	s_nop 0
	v_addc_co_u32_e32 v64, vcc, v64, v67, vcc
	v_cmp_gt_u32_e32 vcc, 8, v64
	s_nop 1
	v_cndmask_b32_e32 v65, 0, v164, vcc
	s_nop 1
	v_add_f32_dpp v65, v65, v65 row_shr:1 row_mask:0xf bank_mask:0xf bound_ctrl:1
	s_nop 1
	v_add_f32_dpp v65, v65, v65 row_shr:2 row_mask:0xf bank_mask:0xf bound_ctrl:1
	s_nop 1
	v_add_f32_dpp v65, v65, v65 row_shr:4 row_mask:0xf bank_mask:0xf bound_ctrl:1
	s_nop 1
	v_add_f32_dpp v65, v65, v65 row_shr:8 row_mask:0xf bank_mask:0xf bound_ctrl:1
	s_nop 1
	v_mov_b32_dpp v66, v65 row_bcast:15 row_mask:0xa bank_mask:0xf
	v_add_f32_e32 v65, v65, v66
	v_mov_b32_e32 v66, v181
	s_nop 1
	v_mov_b32_dpp v66, v65 row_bcast:31 row_mask:0xc bank_mask:0xf
	v_add_f32_e32 v65, v65, v66
	s_nop 0
	v_readlane_b32 s3, v65, 63
	s_and_saveexec_b64 s[0:1], vcc
	s_cbranch_execz .LBB0_1285
	ds_add_u32 v223, v216
	v_mov_b32_e32 v162, v64
	s_branch .LBB0_1285
